# speedup vs baseline: 1.0208x; 1.0208x over previous
.Lu2w_done:
	s_barrier
	s_lshr_b32 s26, s23, 6
	s_mov_b32 s5, 0
	s_add_i32 s27, s27, 0x18000
	v_mov_b32_e32 v15, 0
	v_cmp_neq_f32_e64 s[2:3], 0, v192
	s_andn2_b64 vcc, exec, s[16:17]
	s_mov_b32 s18, 1
	s_cbranch_vccnz .LBB1_86
	s_cmp_eq_u64 s[2:3], 0
	s_cselect_b64 s[2:3], -1, 0
	s_lshl_b32 s4, s26, 2
	s_and_b32 s4, s4, 4
	s_lshl_b32 s19, s25, 14
	s_lshl_b32 s29, s26, 10
	s_cmp_lg_u32 0, -1
	v_bitop3_b32 v0, s4, v200, v208 bitop3:0x36
	s_cselect_b32 s4, 0, 0
	v_lshl_or_b32 v48, s26, 3, v193
	v_mov_b32_e32 v49, 0
	v_or_b32_e32 v4, s19, v1
	s_add_i32 s29, s29, s4
	v_lshlrev_b64 v[2:3], 11, v[48:49]
	s_add_i32 s16, s30, 0x4000
	v_lshlrev_b32_e32 v48, 1, v4
	s_lshl_b32 s4, s24, 6
	s_add_i32 s31, s29, 0xc000
	v_lshl_add_u64 v[4:5], s[14:15], 0, v[48:49]
	s_cmpk_lg_u32 s30, 0x8000
	v_lshl_add_u64 v[2:3], s[6:7], 0, v[2:3]
	v_lshl_add_u64 v[4:5], v[4:5], 0, s[4:5]
	v_lshlrev_b32_e32 v48, 4, v0
	s_cselect_b32 s35, s16, 0
	s_min_u32 s4, s33, 3
	v_lshl_add_u64 v[194:195], v[2:3], 0, v[48:49]
	s_lshl_b32 s4, s4, 18
	v_lshl_add_u64 v[2:3], v[194:195], 0, s[4:5]
	s_add_i32 s4, s29, s30
	s_mov_b32 m0, s4
	s_nop 0
	global_load_lds_dwordx4 v[2:3], off
	s_mov_b64 s[6:7], 0x20000
	v_mov_b32_e32 v191, v49
	v_lshl_add_u64 v[2:3], v[2:3], 0, s[6:7]
	s_addk_i32 s4, 0x2000
	s_mov_b32 m0, s4
	s_nop 0
	global_load_lds_dwordx4 v[2:3], off
	v_lshl_add_u64 v[190:191], v[4:5], 0, v[190:191]
	s_mov_b64 s[14:15], 0x40000
	v_lshl_add_u64 v[2:3], v[190:191], 0, s[14:15]
	s_add_i32 s4, s31, s35
	s_mov_b32 m0, s4
	s_nop 0
	global_load_lds_dwordx4 v[2:3], off
	s_mov_b64 s[16:17], 0x60000
	v_lshl_add_u64 v[2:3], v[190:191], 0, s[16:17]
	v_add_u32_e32 v0, s35, v199
	s_addk_i32 s4, 0x2000
	s_mov_b32 m0, s4
	s_nop 0
	global_load_lds_dwordx4 v[2:3], off
	v_add_u32_e32 v2, v0, v207
	ds_read_b128 v[80:83], v2
	ds_read_b128 v[96:99], v2 offset:4096
	v_add_u32_e32 v2, v0, v206
	ds_read_b128 v[164:167], v2
	ds_read_b128 v[160:163], v2 offset:4096
	v_add_u32_e32 v2, v0, v205
	v_add_u32_e32 v0, v0, v204
	ds_read_b128 v[156:159], v2
	ds_read_b128 v[152:155], v2 offset:4096
	ds_read_b128 v[148:151], v0
	ds_read_b128 v[144:147], v0 offset:4096
	s_add_i32 s4, s35, 0x4000
	s_waitcnt vmcnt(4) lgkmcnt(0)
	s_barrier
	s_cmpk_lg_u32 s35, 0x8000
	s_cselect_b32 s28, s4, 0
	s_cmp_lt_u32 s33, 3
	s_cbranch_scc1 .LBB1_87
	s_lshr_b32 s4, s23, 2
	s_and_b32 s4, s4, 0x3fffffc0
	s_add_u32 s20, s12, s4
	s_addc_u32 s21, s13, 0
	v_lshl_add_u64 v[2:3], s[20:21], 0, v[188:189]
	v_add_lshl_u32 v48, s19, v1, 1
	s_add_u32 s8, s8, s34
	v_lshl_add_u64 v[0:1], v[2:3], 0, v[48:49]
	s_addc_u32 s9, s9, 0
	v_lshl_add_u64 v[0:1], s[8:9], 0, v[0:1]
	s_mov_b64 s[8:9], 0x80000
	v_mov_b32_e32 v48, v49
	v_lshl_add_u64 v[180:181], v[0:1], 0, s[8:9]
	v_mov_b32_e32 v50, v49
	v_mov_b32_e32 v51, v49
	v_mov_b32_e32 v52, v49
	v_mov_b32_e32 v53, v49
	v_mov_b32_e32 v54, v49
	v_mov_b32_e32 v55, v49
	v_mov_b32_e32 v56, v49
	v_mov_b32_e32 v57, v49
	v_mov_b32_e32 v58, v49
	v_mov_b32_e32 v59, v49
	v_mov_b32_e32 v60, v49
	v_mov_b32_e32 v61, v49
	v_mov_b32_e32 v62, v49
	v_mov_b32_e32 v63, v49
	v_mov_b64_e32 v[16:17], v[48:49]
	v_mov_b64_e32 v[0:1], v[48:49]
	v_lshl_add_u32 v182, v202, 2, s27
	v_lshl_add_u32 v183, v203, 2, s27
	s_mov_b32 s36, 5
	s_mov_b32 s34, 0x41000000
	v_mov_b32_e32 v184, 0xff800000
	v_mov_b64_e32 v[18:19], v[50:51]
	v_mov_b64_e32 v[20:21], v[52:53]
	v_mov_b64_e32 v[22:23], v[54:55]
	v_mov_b64_e32 v[24:25], v[56:57]
	v_mov_b64_e32 v[26:27], v[58:59]
	v_mov_b64_e32 v[28:29], v[60:61]
	v_mov_b64_e32 v[30:31], v[62:63]
	v_mov_b64_e32 v[2:3], v[50:51]
	v_mov_b64_e32 v[4:5], v[52:53]
	v_mov_b64_e32 v[6:7], v[54:55]
	v_mov_b64_e32 v[8:9], v[56:57]
	v_mov_b64_e32 v[10:11], v[58:59]
	v_mov_b64_e32 v[12:13], v[60:61]
	v_mov_b64_e32 v[14:15], v[62:63]

.LBB1_135:
	v_mov_b32_e32 v32, 0xff800000
	v_cmp_neq_f32_e32 vcc, 0, v80
	s_nop 1
	v_cndmask_b32_e32 v80, v32, v80, vcc
	v_cmp_neq_f32_e32 vcc, 0, v96
	s_nop 1
	v_cndmask_b32_e32 v96, v32, v96, vcc
	v_cmp_neq_f32_e32 vcc, 0, v81
	s_nop 1
	v_cndmask_b32_e32 v81, v32, v81, vcc
	v_cmp_neq_f32_e32 vcc, 0, v97
	s_nop 1
	v_cndmask_b32_e32 v97, v32, v97, vcc
	v_cmp_neq_f32_e32 vcc, 0, v82
	s_nop 1
	v_cndmask_b32_e32 v82, v32, v82, vcc
	v_cmp_neq_f32_e32 vcc, 0, v98
	s_nop 1
	v_cndmask_b32_e32 v98, v32, v98, vcc
	v_cmp_neq_f32_e32 vcc, 0, v83
	s_nop 1
	v_cndmask_b32_e32 v83, v32, v83, vcc
	v_cmp_neq_f32_e32 vcc, 0, v99
	s_nop 1
	v_cndmask_b32_e32 v99, v32, v99, vcc
	v_cmp_neq_f32_e32 vcc, 0, v84
	s_nop 1
	v_cndmask_b32_e32 v84, v32, v84, vcc
	v_cmp_neq_f32_e32 vcc, 0, v100
	s_nop 1
	v_cndmask_b32_e32 v100, v32, v100, vcc
	v_cmp_neq_f32_e32 vcc, 0, v85
	s_nop 1
	v_cndmask_b32_e32 v85, v32, v85, vcc
	v_cmp_neq_f32_e32 vcc, 0, v101
	s_nop 1
	v_cndmask_b32_e32 v101, v32, v101, vcc
	v_cmp_neq_f32_e32 vcc, 0, v86
	s_nop 1
	v_cndmask_b32_e32 v86, v32, v86, vcc
	v_cmp_neq_f32_e32 vcc, 0, v102
	s_nop 1
	v_cndmask_b32_e32 v102, v32, v102, vcc
	v_cmp_neq_f32_e32 vcc, 0, v87
	s_nop 1
	v_cndmask_b32_e32 v87, v32, v87, vcc
	v_cmp_neq_f32_e32 vcc, 0, v103
	s_nop 1
	v_cndmask_b32_e32 v103, v32, v103, vcc
	v_cmp_neq_f32_e32 vcc, 0, v88
	s_nop 1
	v_cndmask_b32_e32 v88, v32, v88, vcc
	v_cmp_neq_f32_e32 vcc, 0, v104
	s_nop 1
	v_cndmask_b32_e32 v104, v32, v104, vcc
	v_cmp_neq_f32_e32 vcc, 0, v89
	s_nop 1
	v_cndmask_b32_e32 v89, v32, v89, vcc
	v_cmp_neq_f32_e32 vcc, 0, v105
	s_nop 1
	v_cndmask_b32_e32 v105, v32, v105, vcc
	v_cmp_neq_f32_e32 vcc, 0, v90
	s_nop 1
	v_cndmask_b32_e32 v90, v32, v90, vcc
	v_cmp_neq_f32_e32 vcc, 0, v106
	s_nop 1
	v_cndmask_b32_e32 v106, v32, v106, vcc
	v_cmp_neq_f32_e32 vcc, 0, v91
	s_nop 1
	v_cndmask_b32_e32 v91, v32, v91, vcc
	v_cmp_neq_f32_e32 vcc, 0, v107
	s_nop 1
	v_cndmask_b32_e32 v107, v32, v107, vcc
	v_cmp_neq_f32_e32 vcc, 0, v92
	s_nop 1
	v_cndmask_b32_e32 v92, v32, v92, vcc
	v_cmp_neq_f32_e32 vcc, 0, v108
	s_nop 1
	v_cndmask_b32_e32 v108, v32, v108, vcc
	v_cmp_neq_f32_e32 vcc, 0, v93
	s_nop 1
	v_cndmask_b32_e32 v93, v32, v93, vcc
	v_cmp_neq_f32_e32 vcc, 0, v109
	s_nop 1
	v_cndmask_b32_e32 v109, v32, v109, vcc
	v_cmp_neq_f32_e32 vcc, 0, v94
	s_nop 1
	v_cndmask_b32_e32 v94, v32, v94, vcc
	v_cmp_neq_f32_e32 vcc, 0, v110
	s_nop 1
	v_cndmask_b32_e32 v110, v32, v110, vcc
	v_cmp_neq_f32_e32 vcc, 0, v95
	s_nop 1
	v_cndmask_b32_e32 v95, v32, v95, vcc
	v_cmp_neq_f32_e32 vcc, 0, v111
	s_nop 1
	v_cndmask_b32_e32 v111, v32, v111, vcc
	s_branch .LBB1_93
	s_nop 0
	s_nop 0
	s_nop 0
	s_nop 0
	s_nop 0
	s_nop 0
	s_nop 0
	s_endpgm
